# baseline (speedup 1.0000x reference)
.LBB0_21:
	s_mov_b64 exec, -1
	v_readfirstlane_b32 s4, v14
	s_cmp_gt_u32 s4, 0x3fff
	s_cbranch_scc1 .Lprep_end
	s_getpc_b64 s[4:5]
	s_add_u32 s4, s4, 0x4ac
	s_addc_u32 s5, s5, 0
	v_lshlrev_b32_e32 v37, 4, v28
	global_load_dwordx4 v[38:41], v37, s[4:5]
	global_load_dwordx4 v[38:41], v37, s[4:5] offset:1024
	global_load_dwordx4 v[38:41], v37, s[4:5] offset:2048
	global_load_dwordx4 v[38:41], v37, s[4:5] offset:3072
	s_add_u32 s4, s4, 0x1000
	s_addc_u32 s5, s5, 0
	global_load_dwordx4 v[38:41], v37, s[4:5]
	global_load_dwordx4 v[38:41], v37, s[4:5] offset:1024

	.amdhsa_kernel _Z11prep_kernelPKfS0_S0_S0_S0_S0_S0_PKiPc
		.amdhsa_group_segment_fixed_size 256
		.amdhsa_private_segment_fixed_size 0
		.amdhsa_kernarg_size 328
		.amdhsa_user_sgpr_count 2
		.amdhsa_user_sgpr_dispatch_ptr 0
		.amdhsa_user_sgpr_queue_ptr 0
		.amdhsa_user_sgpr_kernarg_segment_ptr 1
		.amdhsa_user_sgpr_dispatch_id 0
		.amdhsa_user_sgpr_kernarg_preload_length 0
		.amdhsa_user_sgpr_kernarg_preload_offset 0
		.amdhsa_user_sgpr_private_segment_size 0
		.amdhsa_uses_dynamic_stack 0
		.amdhsa_enable_private_segment 0
		.amdhsa_system_sgpr_workgroup_id_x 1
		.amdhsa_system_sgpr_workgroup_id_y 0
		.amdhsa_system_sgpr_workgroup_id_z 0
		.amdhsa_system_sgpr_workgroup_info 0
		.amdhsa_system_vgpr_workitem_id 2
		.amdhsa_next_free_vgpr 42
		.amdhsa_next_free_sgpr 52
		.amdhsa_accum_offset 44
		.amdhsa_reserve_vcc 1
		.amdhsa_float_round_mode_32 0
		.amdhsa_float_round_mode_16_64 0
		.amdhsa_float_denorm_mode_32 3
		.amdhsa_float_denorm_mode_16_64 3
		.amdhsa_dx10_clamp 1
		.amdhsa_ieee_mode 1
		.amdhsa_fp16_overflow 0
		.amdhsa_tg_split 0
		.amdhsa_exception_fp_ieee_invalid_op 0
		.amdhsa_exception_fp_denorm_src 0
		.amdhsa_exception_fp_ieee_div_zero 0
		.amdhsa_exception_fp_ieee_overflow 0
		.amdhsa_exception_fp_ieee_underflow 0
		.amdhsa_exception_fp_ieee_inexact 0
		.amdhsa_exception_int_div_zero 0
	.end_amdhsa_kernel

.LBB1_53:
	s_waitcnt vmcnt(0)
	v_cmp_ne_u32_e32 vcc, 0, v0
	s_lshr_b32 s0, vcc_lo, 16
	s_lshr_b32 s1, vcc_hi, 16
	s_or_b32 s0, s0, vcc_lo
	s_or_b32 s1, s1, vcc_hi
	s_or_b32 s0, s0, s1
	s_and_b32 s0, s0, 0xffff
	s_cmp_eq_u32 s0, 0
	s_cbranch_scc1 .LBB1_104
	s_cmp_lg_u32 s33, 0
	s_cbranch_scc1 .Lfl_nopf
	s_getpc_b64 s[26:27]
	s_add_u32 s26, s26, 0x368
	s_addc_u32 s27, s27, 0
	v_lshlrev_b32_e32 v78, 4, v101
	global_load_dwordx4 v[80:83], v78, s[26:27]
	global_load_dwordx4 v[84:87], v78, s[26:27] offset:1024
	global_load_dwordx4 v[88:91], v78, s[26:27] offset:2048
	global_load_dwordx4 v[92:95], v78, s[26:27] offset:3072
.Lfl_nopf:
	v_lshrrev_b32_e64 v1, v100, s0
	v_and_b32_e32 v3, 15, v101
	v_and_b32_e32 v1, 1, v1
	v_add_u32_e32 v2, s16, v3
	v_cmp_ne_u32_e64 s[2:3], 0, v1
	v_cmp_eq_u32_e64 s[6:7], s45, v2
	v_cmp_eq_u32_e64 s[8:9], s46, v2
	s_and_b32 s38, s2, 0xffff
	s_flbit_i32_b32 s4, s38
	s_sub_u32 s5, 31, s4
	s_or_b64 s[6:7], s[6:7], s[8:9]
	v_cmp_le_u32_e64 s[12:13], s5, v3
	s_or_b64 s[6:7], s[6:7], s[20:21]
	v_add3_u32 v3, s33, v105, v102
	s_or_b64 s[6:7], s[6:7], s[12:13]
	s_and_b32 s1, s6, s38
	s_andn2_b32 s3, s38, s1
	v_add_u32_e32 v36, 0x8000, v3
	v_add_u32_e32 v37, 0x8800, v3
	v_add_u32_e32 v38, 0x9000, v3
	v_add_u32_e32 v39, 0x9800, v3
	ds_write2_b32 v36, v32, v28 offset1:16
	ds_write2_b32 v36, v24, v20 offset0:32 offset1:48
	ds_write2_b32 v36, v16, v12 offset0:64 offset1:80
	ds_write2_b32 v36, v8, v4 offset0:96 offset1:112
	ds_write2_b32 v37, v33, v29 offset1:16
	ds_write2_b32 v37, v25, v21 offset0:32 offset1:48
	ds_write2_b32 v37, v17, v13 offset0:64 offset1:80
	ds_write2_b32 v37, v9, v5 offset0:96 offset1:112
	ds_write2_b32 v38, v34, v30 offset1:16
	ds_write2_b32 v38, v26, v22 offset0:32 offset1:48
	ds_write2_b32 v38, v18, v14 offset0:64 offset1:80
	ds_write2_b32 v38, v10, v6 offset0:96 offset1:112
	ds_write2_b32 v39, v35, v31 offset1:16
	ds_write2_b32 v39, v27, v23 offset0:32 offset1:48
	ds_write2_b32 v39, v19, v15 offset0:64 offset1:80
	ds_write2_b32 v39, v11, v7 offset0:96 offset1:112
	s_mov_b32 s17, 0
	s_lshl_b64 s[14:15], s[16:17], 9
	s_add_u32 s14, s18, s14
	s_addc_u32 s15, s19, s15
	s_add_u32 s22, s14, 0x1000
	s_addc_u32 s23, s15, 0
	v_lshlrev_b32_e32 v40, 2, v101
	v_add_u32_e32 v41, s33, v40
	v_and_b32_e32 v2, 31, v101
	v_lshrrev_b32_e32 v1, 5, v101
	v_lshlrev_b32_e32 v2, 4, v2
	v_lshl_add_u32 v42, v1, 9, v2
	v_add_u32_e32 v43, s33, v42
	v_lshrrev_b32_e64 v76, v1, s3
	s_waitcnt lgkmcnt(0)
	ds_read_b128 v[44:47], v43 offset:32768
	ds_read_b128 v[48:51], v43 offset:33792
	ds_read_b128 v[52:55], v43 offset:34816
	ds_read_b128 v[56:59], v43 offset:35840
	ds_read_b128 v[60:63], v43 offset:36864
	ds_read_b128 v[64:67], v43 offset:37888
	ds_read_b128 v[68:71], v43 offset:38912
	ds_read_b128 v[72:75], v43 offset:39936
	v_cmp_ne_u32_e32 vcc, 0, v0
	s_and_saveexec_b64 s[24:25], vcc
	s_cbranch_execz .Lfl_nocnt
	s_mov_b32 s2, 0x24924925
	v_mul_hi_u32 v1, v0, s2
	v_sub_u32_e32 v0, v0, v1
	v_lshrrev_b32_e32 v0, 1, v0
	v_add_u32_e32 v0, v0, v1
	v_lshrrev_b32_e32 v0, 2, v0
	v_cvt_f32_u32_e32 v0, v0
	s_lshl_b64 s[26:27], s[16:17], 2
	s_add_u32 s26, s10, s26
	s_addc_u32 s27, s11, s27
	v_lshlrev_b32_e32 v1, 2, v100
	global_atomic_add_f32 v1, v0, s[26:27]

amdhsa.kernels:
  - .agpr_count:     0
    .args:
      - .actual_access:  read_only
        .address_space:  global
        .offset:         0
        .size:           8
        .value_kind:     global_buffer
      - .actual_access:  read_only
        .address_space:  global
        .offset:         8
        .size:           8
        .value_kind:     global_buffer
      - .actual_access:  read_only
        .address_space:  global
        .offset:         16
        .size:           8
        .value_kind:     global_buffer
      - .actual_access:  read_only
        .address_space:  global
        .offset:         24
        .size:           8
        .value_kind:     global_buffer
      - .actual_access:  read_only
        .address_space:  global
        .offset:         32
        .size:           8
        .value_kind:     global_buffer
      - .actual_access:  read_only
        .address_space:  global
        .offset:         40
        .size:           8
        .value_kind:     global_buffer
      - .actual_access:  read_only
        .address_space:  global
        .offset:         48
        .size:           8
        .value_kind:     global_buffer
      - .actual_access:  read_only
        .address_space:  global
        .offset:         56
        .size:           8
        .value_kind:     global_buffer
      - .address_space:  global
        .offset:         64
        .size:           8
        .value_kind:     global_buffer
      - .offset:         72
        .size:           4
        .value_kind:     hidden_block_count_x
      - .offset:         76
        .size:           4
        .value_kind:     hidden_block_count_y
      - .offset:         80
        .size:           4
        .value_kind:     hidden_block_count_z
      - .offset:         84
        .size:           2
        .value_kind:     hidden_group_size_x
      - .offset:         86
        .size:           2
        .value_kind:     hidden_group_size_y
      - .offset:         88
        .size:           2
        .value_kind:     hidden_group_size_z
      - .offset:         90
        .size:           2
        .value_kind:     hidden_remainder_x
      - .offset:         92
        .size:           2
        .value_kind:     hidden_remainder_y
      - .offset:         94
        .size:           2
        .value_kind:     hidden_remainder_z
      - .offset:         112
        .size:           8
        .value_kind:     hidden_global_offset_x
      - .offset:         120
        .size:           8
        .value_kind:     hidden_global_offset_y
      - .offset:         128
        .size:           8
        .value_kind:     hidden_global_offset_z
      - .offset:         136
        .size:           2
        .value_kind:     hidden_grid_dims
    .group_segment_fixed_size: 256
    .kernarg_segment_align: 8
    .kernarg_segment_size: 328
    .language:       OpenCL C
    .language_version:
      - 2
      - 0
    .max_flat_workgroup_size: 256
    .name:           _Z11prep_kernelPKfS0_S0_S0_S0_S0_S0_PKiPc
    .private_segment_fixed_size: 0
    .sgpr_count:     58
    .sgpr_spill_count: 0
    .symbol:         _Z11prep_kernelPKfS0_S0_S0_S0_S0_S0_PKiPc.kd
    .uniform_work_group_size: 1
    .uses_dynamic_stack: false
    .vgpr_count:     42
    .vgpr_spill_count: 0
    .wavefront_size: 64
  - .agpr_count:     0
    .args:
      - .actual_access:  read_only
        .address_space:  global
        .offset:         0
        .size:           8
        .value_kind:     global_buffer
      - .address_space:  global
        .offset:         8
        .size:           8
        .value_kind:     global_buffer
      - .actual_access:  read_only
        .address_space:  global
        .offset:         16
        .size:           8
        .value_kind:     global_buffer
      - .actual_access:  read_only
        .address_space:  global
        .offset:         24
        .size:           8
        .value_kind:     global_buffer
      - .address_space:  global
        .offset:         32
        .size:           8
        .value_kind:     global_buffer
      - .address_space:  global
        .offset:         40
        .size:           8
        .value_kind:     global_buffer
      - .actual_access:  read_only
        .address_space:  global
        .offset:         48
        .size:           8
        .value_kind:     global_buffer
      - .offset:         56
        .size:           4
        .value_kind:     by_value
      - .offset:         64
        .size:           4
        .value_kind:     hidden_block_count_x
      - .offset:         68
        .size:           4
        .value_kind:     hidden_block_count_y
      - .offset:         72
        .size:           4
        .value_kind:     hidden_block_count_z
      - .offset:         76
        .size:           2
        .value_kind:     hidden_group_size_x
      - .offset:         78
        .size:           2
        .value_kind:     hidden_group_size_y
      - .offset:         80
        .size:           2
        .value_kind:     hidden_group_size_z
      - .offset:         82
        .size:           2
        .value_kind:     hidden_remainder_x
      - .offset:         84
        .size:           2
        .value_kind:     hidden_remainder_y
      - .offset:         86
        .size:           2
        .value_kind:     hidden_remainder_z
      - .offset:         104
        .size:           8
        .value_kind:     hidden_global_offset_x
      - .offset:         112
        .size:           8
        .value_kind:     hidden_global_offset_y
      - .offset:         120
        .size:           8
        .value_kind:     hidden_global_offset_z
      - .offset:         128
        .size:           2
        .value_kind:     hidden_grid_dims
    .group_segment_fixed_size: 135936
    .kernarg_segment_align: 8
    .kernarg_segment_size: 320
    .language:       OpenCL C
    .language_version:
      - 2
      - 0
    .max_flat_workgroup_size: 768
    .name:           _Z11main_kernelPKfPKiPK15HIP_vector_typeIjLj4EES0_PfS7_S2_i
    .private_segment_fixed_size: 0
    .sgpr_count:     66
    .sgpr_spill_count: 0
    .symbol:         _Z11main_kernelPKfPKiPK15HIP_vector_typeIjLj4EES0_PfS7_S2_i.kd
    .uniform_work_group_size: 1
    .uses_dynamic_stack: false
    .vgpr_count:     168
    .vgpr_spill_count: 0
    .wavefront_size: 64
  - .agpr_count:     60
    .args:
      - .actual_access:  read_only
        .address_space:  global
        .offset:         0
        .size:           8
        .value_kind:     global_buffer
      - .actual_access:  read_only
        .address_space:  global
        .offset:         8
        .size:           8
        .value_kind:     global_buffer
      - .actual_access:  read_only
        .address_space:  global
        .offset:         16
        .size:           8
        .value_kind:     global_buffer
      - .actual_access:  read_only
        .address_space:  global
        .offset:         24
        .size:           8
        .value_kind:     global_buffer
      - .actual_access:  read_only
        .address_space:  global
        .offset:         32
        .size:           8
        .value_kind:     global_buffer
      - .actual_access:  read_only
        .address_space:  global
        .offset:         40
        .size:           8
        .value_kind:     global_buffer
      - .actual_access:  read_only
        .address_space:  global
        .offset:         48
        .size:           8
        .value_kind:     global_buffer
      - .actual_access:  read_only
        .address_space:  global
        .offset:         56
        .size:           8
        .value_kind:     global_buffer
      - .address_space:  global
        .offset:         64
        .size:           8
        .value_kind:     global_buffer
    .group_segment_fixed_size: 86272
    .kernarg_segment_align: 8
    .kernarg_segment_size: 72
    .language:       OpenCL C
    .language_version:
      - 2
      - 0
    .max_flat_workgroup_size: 256
    .name:           _Z10enc_kernelPKfS0_PK15HIP_vector_typeIjLj4EES4_S4_S0_S0_S0_Pf
    .private_segment_fixed_size: 0
    .sgpr_count:     24
    .sgpr_spill_count: 0
    .symbol:         _Z10enc_kernelPKfS0_PK15HIP_vector_typeIjLj4EES4_S4_S0_S0_S0_Pf.kd
    .uniform_work_group_size: 1
    .uses_dynamic_stack: false
    .vgpr_count:     252
    .vgpr_spill_count: 0
    .wavefront_size: 64
